# phase 5c as a 2-row software-pipelined loop (small code footprint) on top of v24
# baseline (speedup 1.0000x reference)
; DEV int ltid() { int t = threadIdx.x; asm volatile("" : "+v"(t)); return t; }
; DEV float bflo(unsigned v) { return __uint_as_float(v << 16); }
; DEV float bfhi(unsigned v) { return __uint_as_float(v & 0xffff0000u); }
; DEV void phase5c_rec(CParams& p, int wg, int nwg) {
;   const int wid = ltid() >> 6, lane = ltid() & 63;
;   for (int row = wg * 8 + wid; row < NLAT; row += nwg * 8) {
;     const bf16_t* a = p.of + (long)row * 1024 + lane * 16; const bf16_t* b = p.ob + (long)row * 1024 + lane * 16;
;     const u32x4 a0 = *(const u32x4*)a, a1 = *(const u32x4*)(a + 8), b0 = *(const u32x4*)b, b1 = *(const u32x4*)(b + 8);
;     const unsigned aw[8] = {a0.x, a0.y, a0.z, a0.w, a1.x, a1.y, a1.z, a1.w}, bw[8] = {b0.x, b0.y, b0.z, b0.w, b1.x, b1.y, b1.z, b1.w};
;     float v[16]; float ss = 0.f;
; #pragma unroll
;     for (int i = 0; i < 8; ++i) { v[2 * i] = bflo(aw[i]) + bflo(bw[i]); v[2 * i + 1] = bfhi(aw[i]) + bfhi(bw[i]); ss += v[2 * i] * v[2 * i] + v[2 * i + 1] * v[2 * i + 1]; }
;     ss += __shfl_xor(ss, 1); ss += __shfl_xor(ss, 2); ss += __shfl_xor(ss, 4);
.LBB0_1183:
	s_or_b64 exec, exec, s[4:5]
	s_mov_b64 s[10:11], s[0:1]
	s_waitcnt lgkmcnt(0)
	v_mov_b32_e32 v1, v0
	s_barrier
	s_mov_b64 s[8:9], exec
	s_load_dwordx4 s[4:7], s[0:1], 0x188
	s_load_dwordx2 s[12:13], s[0:1], 0x198
	s_load_dwordx2 s[14:15], s[0:1], 0x168
	s_load_dwordx2 s[16:17], s[0:1], 0x80
	v_mbcnt_lo_u32_b32 v208, -1, 0
	v_mbcnt_hi_u32_b32 v208, -1, v208
	v_lshlrev_b32_e32 v1, 4, v208
	v_xor_b32_e32 v2, 1, v208
	v_lshlrev_b32_e32 v2, 2, v2
	v_xor_b32_e32 v3, 2, v208
	v_lshlrev_b32_e32 v3, 2, v3
	v_xor_b32_e32 v4, 4, v208
	v_lshlrev_b32_e32 v4, 2, v4
	v_xor_b32_e32 v5, 8, v208
	v_lshlrev_b32_e32 v5, 2, v5
	v_and_b32_e32 v209, 15, v208
	v_lshlrev_b32_e32 v209, 5, v209
	v_lshrrev_b32_e32 v210, 6, v0
	s_nop 0
	v_readfirstlane_b32 s22, v210
	s_nop 3
	s_add_i32 s20, s75, s22
	s_lshl_b32 s21, s33, 3
	s_waitcnt lgkmcnt(0)
	global_load_dwordx4 v[6:9], v209, s[16:17]
	global_load_dwordx4 v[10:13], v209, s[16:17] offset:16
	s_cmp_lt_u32 s20, 0x4000
	s_cbranch_scc0 .Lp5c_end
	s_lshl_b32 s22, s20, 11
	s_add_u32 s24, s6, s22
	s_addc_u32 s25, s7, 0
	s_add_u32 s26, s12, s22
	s_addc_u32 s27, s13, 0
	s_add_u32 s28, s14, s22
	s_addc_u32 s29, s15, 0
	s_add_u32 s28, s28, 0x200000
	s_addc_u32 s29, s29, 0
	global_load_dwordx4 v[16:19], v1, s[24:25] offset:0
	global_load_dwordx4 v[20:23], v1, s[24:25] offset:1024
	global_load_dwordx4 v[24:27], v1, s[26:27] offset:0
	global_load_dwordx4 v[28:31], v1, s[26:27] offset:1024
	global_load_dwordx4 v[32:35], v1, s[28:29] offset:0
	global_load_dwordx4 v[36:39], v1, s[28:29] offset:1024
.Lp5c_a:
	s_add_u32 s23, s20, s21
	s_cmp_lt_u32 s23, 0x4000
	s_cbranch_scc0 .Lp5c_a_last
	s_lshl_b32 s22, s23, 11
	s_add_u32 s24, s6, s22
	s_addc_u32 s25, s7, 0
	s_add_u32 s26, s12, s22
	s_addc_u32 s27, s13, 0
	s_add_u32 s28, s14, s22
	s_addc_u32 s29, s15, 0
	s_add_u32 s28, s28, 0x200000
	s_addc_u32 s29, s29, 0
	global_load_dwordx4 v[40:43], v1, s[24:25] offset:0
	global_load_dwordx4 v[44:47], v1, s[24:25] offset:1024
	global_load_dwordx4 v[48:51], v1, s[26:27] offset:0
	global_load_dwordx4 v[52:55], v1, s[26:27] offset:1024
	global_load_dwordx4 v[56:59], v1, s[28:29] offset:0
	global_load_dwordx4 v[60:63], v1, s[28:29] offset:1024
	s_waitcnt vmcnt(6)
	v_lshlrev_b32_e32 v208, 16, v16
	v_lshlrev_b32_e32 v209, 16, v24
	v_and_b32_e32 v210, 0xffff0000, v16
	v_and_b32_e32 v211, 0xffff0000, v24
	v_add_f32_e32 v16, v208, v209
	v_add_f32_e32 v24, v210, v211
	v_lshlrev_b32_e32 v208, 16, v17
	v_lshlrev_b32_e32 v209, 16, v25
	v_and_b32_e32 v210, 0xffff0000, v17
	v_and_b32_e32 v211, 0xffff0000, v25
	v_add_f32_e32 v17, v208, v209
	v_add_f32_e32 v25, v210, v211
	v_lshlrev_b32_e32 v208, 16, v18
	v_lshlrev_b32_e32 v209, 16, v26
	v_and_b32_e32 v210, 0xffff0000, v18
	v_and_b32_e32 v211, 0xffff0000, v26
	v_add_f32_e32 v18, v208, v209
	v_add_f32_e32 v26, v210, v211
	v_lshlrev_b32_e32 v208, 16, v19
	v_lshlrev_b32_e32 v209, 16, v27
	v_and_b32_e32 v210, 0xffff0000, v19
	v_and_b32_e32 v211, 0xffff0000, v27
	v_add_f32_e32 v19, v208, v209
	v_add_f32_e32 v27, v210, v211
	v_mul_f32_e32 v212, v16, v16
	v_fmac_f32_e32 v212, v24, v24
	v_fmac_f32_e32 v212, v17, v17
	v_fmac_f32_e32 v212, v25, v25
	v_fmac_f32_e32 v212, v18, v18
	v_fmac_f32_e32 v212, v26, v26
	v_fmac_f32_e32 v212, v19, v19
	v_fmac_f32_e32 v212, v27, v27
	v_lshlrev_b32_e32 v208, 16, v20
	v_lshlrev_b32_e32 v209, 16, v28
	v_and_b32_e32 v210, 0xffff0000, v20
	v_and_b32_e32 v211, 0xffff0000, v28
	v_add_f32_e32 v20, v208, v209
	v_add_f32_e32 v28, v210, v211
	v_lshlrev_b32_e32 v208, 16, v21
	v_lshlrev_b32_e32 v209, 16, v29
	v_and_b32_e32 v210, 0xffff0000, v21
	v_and_b32_e32 v211, 0xffff0000, v29
	v_add_f32_e32 v21, v208, v209
	v_add_f32_e32 v29, v210, v211
	v_lshlrev_b32_e32 v208, 16, v22
	v_lshlrev_b32_e32 v209, 16, v30
	v_and_b32_e32 v210, 0xffff0000, v22
	v_and_b32_e32 v211, 0xffff0000, v30
	v_add_f32_e32 v22, v208, v209
	v_add_f32_e32 v30, v210, v211
	v_lshlrev_b32_e32 v208, 16, v23
	v_lshlrev_b32_e32 v209, 16, v31
	v_and_b32_e32 v210, 0xffff0000, v23
	v_and_b32_e32 v211, 0xffff0000, v31
	v_add_f32_e32 v23, v208, v209
	v_add_f32_e32 v31, v210, v211
	v_mul_f32_e32 v213, v20, v20
	v_fmac_f32_e32 v213, v28, v28
	v_fmac_f32_e32 v213, v21, v21
	v_fmac_f32_e32 v213, v29, v29
	v_fmac_f32_e32 v213, v22, v22
	v_fmac_f32_e32 v213, v30, v30
	v_fmac_f32_e32 v213, v23, v23
	v_fmac_f32_e32 v213, v31, v31
	ds_bpermute_b32 v214, v2, v212
	ds_bpermute_b32 v215, v2, v213
	s_waitcnt lgkmcnt(0)
	v_add_f32_e32 v212, v212, v214
	v_add_f32_e32 v213, v213, v215
	ds_bpermute_b32 v214, v3, v212
	ds_bpermute_b32 v215, v3, v213
	s_waitcnt lgkmcnt(0)
	v_add_f32_e32 v212, v212, v214
	v_add_f32_e32 v213, v213, v215
	ds_bpermute_b32 v214, v4, v212
	ds_bpermute_b32 v215, v4, v213
	s_waitcnt lgkmcnt(0)
	v_add_f32_e32 v212, v212, v214
	v_add_f32_e32 v213, v213, v215
	ds_bpermute_b32 v214, v5, v212
	ds_bpermute_b32 v215, v5, v213
	s_waitcnt lgkmcnt(0)
; DEV unsigned cvt_pk_bf16(float lo, float hi) { const f32x2 v = {lo, hi}; const bf16n2 r = __builtin_convertvector(v, bf16n2); return __builtin_bit_cast(unsigned, r); }
; DEV float bflo(unsigned v) { return __uint_as_float(v << 16); }
; DEV float bfhi(unsigned v) { return __uint_as_float(v & 0xffff0000u); }
; DEV void phase5c_rec(CParams& p, int wg, int nwg) {
;     ...
;     ss += __shfl_xor(ss, 1); ss += __shfl_xor(ss, 2); ss += __shfl_xor(ss, 4);
;     const float rstd = rsqrtf(ss * (1.f / DV) + EPS);
;     const bf16_t* gp = p.gate + (long)(NCTX + row) * 1024 + lane * 16;
;     const u32x4 g0 = *(const u32x4*)gp, g1 = *(const u32x4*)(gp + 8);
;     float gt[16]; gt[0] = bflo(g0.x); gt[1] = bfhi(g0.x); gt[2] = bflo(g0.y); gt[3] = bfhi(g0.y); gt[4] = bflo(g0.z); gt[5] = bfhi(g0.z); gt[6] = bflo(g0.w); gt[7] = bfhi(g0.w);
;     gt[8] = bflo(g1.x); gt[9] = bfhi(g1.x); gt[10] = bflo(g1.y); gt[11] = bfhi(g1.y); gt[12] = bflo(g1.z); gt[13] = bfhi(g1.z); gt[14] = bflo(g1.w); gt[15] = bfhi(g1.w);
;     const float* gn = p.g_norm + (lane & 7) * 16;
;     unsigned o[8];
; #pragma unroll
;     for (int j = 0; j < 8; ++j) o[j] = cvt_pk_bf16(v[2 * j] * rstd * gn[2 * j] * gt[2 * j], v[2 * j + 1] * rstd * gn[2 * j + 1] * gt[2 * j + 1]);
;     bf16_t* op = p.aout + (long)row * DM + 1024 + lane * 16;
;     *(u32x4*)op = (u32x4){o[0], o[1], o[2], o[3]}; *(u32x4*)(op + 8) = (u32x4){o[4], o[5], o[6], o[7]};
;   }
	v_add_f32_e32 v212, v212, v214
	v_add_f32_e32 v213, v213, v215
	v_mov_b32_e32 v214, 0x358637bd
	v_fmac_f32_e32 v214, 0x3c000000, v212
	v_mov_b32_e32 v215, 0x358637bd
	v_fmac_f32_e32 v215, 0x3c000000, v213
	v_rsq_f32_e32 v214, v214
	v_rsq_f32_e32 v215, v215
	s_lshl_b32 s22, s20, 12
	s_add_u32 s30, s4, s22
	s_addc_u32 s31, s5, 0
	v_lshlrev_b32_e32 v208, 16, v32
	v_and_b32_e32 v209, 0xffff0000, v32
	v_mul_f32_e32 v16, v16, v214
	v_mul_f32_e32 v24, v24, v214
	v_mul_f32_e32 v16, v16, v6
	v_mul_f32_e32 v24, v24, v7
	v_mul_f32_e32 v16, v16, v208
	v_mul_f32_e32 v24, v24, v209
	v_cvt_pk_bf16_f32 v32, v16, v24
	v_lshlrev_b32_e32 v208, 16, v33
	v_and_b32_e32 v209, 0xffff0000, v33
	v_mul_f32_e32 v17, v17, v214
	v_mul_f32_e32 v25, v25, v214
	v_mul_f32_e32 v17, v17, v8
	v_mul_f32_e32 v25, v25, v9
	v_mul_f32_e32 v17, v17, v208
	v_mul_f32_e32 v25, v25, v209
	v_cvt_pk_bf16_f32 v33, v17, v25
	v_lshlrev_b32_e32 v208, 16, v34
	v_and_b32_e32 v209, 0xffff0000, v34
	v_mul_f32_e32 v18, v18, v214
	v_mul_f32_e32 v26, v26, v214
	v_mul_f32_e32 v18, v18, v10
	v_mul_f32_e32 v26, v26, v11
	v_mul_f32_e32 v18, v18, v208
	v_mul_f32_e32 v26, v26, v209
	v_cvt_pk_bf16_f32 v34, v18, v26
	v_lshlrev_b32_e32 v208, 16, v35
	v_and_b32_e32 v209, 0xffff0000, v35
	v_mul_f32_e32 v19, v19, v214
	v_mul_f32_e32 v27, v27, v214
	v_mul_f32_e32 v19, v19, v12
	v_mul_f32_e32 v27, v27, v13
	v_mul_f32_e32 v19, v19, v208
	v_mul_f32_e32 v27, v27, v209
	v_cvt_pk_bf16_f32 v35, v19, v27
	global_store_dwordx4 v1, v[32:35], s[30:31] offset:2048
	v_lshlrev_b32_e32 v208, 16, v36
	v_and_b32_e32 v209, 0xffff0000, v36
	v_mul_f32_e32 v20, v20, v215
	v_mul_f32_e32 v28, v28, v215
	v_mul_f32_e32 v20, v20, v6
	v_mul_f32_e32 v28, v28, v7
	v_mul_f32_e32 v20, v20, v208
	v_mul_f32_e32 v28, v28, v209
	v_cvt_pk_bf16_f32 v36, v20, v28
	v_lshlrev_b32_e32 v208, 16, v37
	v_and_b32_e32 v209, 0xffff0000, v37
	v_mul_f32_e32 v21, v21, v215
	v_mul_f32_e32 v29, v29, v215
	v_mul_f32_e32 v21, v21, v8
	v_mul_f32_e32 v29, v29, v9
	v_mul_f32_e32 v21, v21, v208
	v_mul_f32_e32 v29, v29, v209
	v_cvt_pk_bf16_f32 v37, v21, v29
	v_lshlrev_b32_e32 v208, 16, v38
	v_and_b32_e32 v209, 0xffff0000, v38
	v_mul_f32_e32 v22, v22, v215
	v_mul_f32_e32 v30, v30, v215
	v_mul_f32_e32 v22, v22, v10
	v_mul_f32_e32 v30, v30, v11
	v_mul_f32_e32 v22, v22, v208
	v_mul_f32_e32 v30, v30, v209
	v_cvt_pk_bf16_f32 v38, v22, v30
	v_lshlrev_b32_e32 v208, 16, v39
	v_and_b32_e32 v209, 0xffff0000, v39
	v_mul_f32_e32 v23, v23, v215
	v_mul_f32_e32 v31, v31, v215
	v_mul_f32_e32 v23, v23, v12
	v_mul_f32_e32 v31, v31, v13
	v_mul_f32_e32 v23, v23, v208
	v_mul_f32_e32 v31, v31, v209
	v_cvt_pk_bf16_f32 v39, v23, v31
	global_store_dwordx4 v1, v[36:39], s[30:31] offset:3072
	s_mov_b32 s20, s23
	s_branch .Lp5c_a_next
.Lp5c_a_last:
	s_waitcnt vmcnt(0)
	v_lshlrev_b32_e32 v208, 16, v16
	v_lshlrev_b32_e32 v209, 16, v24
	v_and_b32_e32 v210, 0xffff0000, v16
	v_and_b32_e32 v211, 0xffff0000, v24
	v_add_f32_e32 v16, v208, v209
	v_add_f32_e32 v24, v210, v211
	v_lshlrev_b32_e32 v208, 16, v17
	v_lshlrev_b32_e32 v209, 16, v25
	v_and_b32_e32 v210, 0xffff0000, v17
	v_and_b32_e32 v211, 0xffff0000, v25
	v_add_f32_e32 v17, v208, v209
	v_add_f32_e32 v25, v210, v211
	v_lshlrev_b32_e32 v208, 16, v18
	v_lshlrev_b32_e32 v209, 16, v26
	v_and_b32_e32 v210, 0xffff0000, v18
	v_and_b32_e32 v211, 0xffff0000, v26
	v_add_f32_e32 v18, v208, v209
	v_add_f32_e32 v26, v210, v211
	v_lshlrev_b32_e32 v208, 16, v19
	v_lshlrev_b32_e32 v209, 16, v27
	v_and_b32_e32 v210, 0xffff0000, v19
	v_and_b32_e32 v211, 0xffff0000, v27
	v_add_f32_e32 v19, v208, v209
	v_add_f32_e32 v27, v210, v211
	v_mul_f32_e32 v212, v16, v16
	v_fmac_f32_e32 v212, v24, v24
	v_fmac_f32_e32 v212, v17, v17
	v_fmac_f32_e32 v212, v25, v25
	v_fmac_f32_e32 v212, v18, v18
	v_fmac_f32_e32 v212, v26, v26
	v_fmac_f32_e32 v212, v19, v19
	v_fmac_f32_e32 v212, v27, v27
	v_lshlrev_b32_e32 v208, 16, v20
	v_lshlrev_b32_e32 v209, 16, v28
	v_and_b32_e32 v210, 0xffff0000, v20
	v_and_b32_e32 v211, 0xffff0000, v28
	v_add_f32_e32 v20, v208, v209
	v_add_f32_e32 v28, v210, v211
	v_lshlrev_b32_e32 v208, 16, v21
	v_lshlrev_b32_e32 v209, 16, v29
	v_and_b32_e32 v210, 0xffff0000, v21
	v_and_b32_e32 v211, 0xffff0000, v29
	v_add_f32_e32 v21, v208, v209
	v_add_f32_e32 v29, v210, v211
	v_lshlrev_b32_e32 v208, 16, v22
	v_lshlrev_b32_e32 v209, 16, v30
	v_and_b32_e32 v210, 0xffff0000, v22
	v_and_b32_e32 v211, 0xffff0000, v30
	v_add_f32_e32 v22, v208, v209
	v_add_f32_e32 v30, v210, v211
	v_lshlrev_b32_e32 v208, 16, v23
	v_lshlrev_b32_e32 v209, 16, v31
	v_and_b32_e32 v210, 0xffff0000, v23
	v_and_b32_e32 v211, 0xffff0000, v31
	v_add_f32_e32 v23, v208, v209
	v_add_f32_e32 v31, v210, v211
	v_mul_f32_e32 v213, v20, v20
	v_fmac_f32_e32 v213, v28, v28
	v_fmac_f32_e32 v213, v21, v21
	v_fmac_f32_e32 v213, v29, v29
	v_fmac_f32_e32 v213, v22, v22
	v_fmac_f32_e32 v213, v30, v30
	v_fmac_f32_e32 v213, v23, v23
	v_fmac_f32_e32 v213, v31, v31
	ds_bpermute_b32 v214, v2, v212
	ds_bpermute_b32 v215, v2, v213
	s_waitcnt lgkmcnt(0)
	v_add_f32_e32 v212, v212, v214
	v_add_f32_e32 v213, v213, v215
	ds_bpermute_b32 v214, v3, v212
	ds_bpermute_b32 v215, v3, v213
	s_waitcnt lgkmcnt(0)
	v_add_f32_e32 v212, v212, v214
	v_add_f32_e32 v213, v213, v215
	ds_bpermute_b32 v214, v4, v212
	ds_bpermute_b32 v215, v4, v213
	s_waitcnt lgkmcnt(0)
	v_add_f32_e32 v212, v212, v214
	v_add_f32_e32 v213, v213, v215
	ds_bpermute_b32 v214, v5, v212
	ds_bpermute_b32 v215, v5, v213
	s_waitcnt lgkmcnt(0)
; DEV unsigned cvt_pk_bf16(float lo, float hi) { const f32x2 v = {lo, hi}; const bf16n2 r = __builtin_convertvector(v, bf16n2); return __builtin_bit_cast(unsigned, r); }
; DEV float bflo(unsigned v) { return __uint_as_float(v << 16); }
; DEV float bfhi(unsigned v) { return __uint_as_float(v & 0xffff0000u); }
; DEV void phase5c_rec(CParams& p, int wg, int nwg) {
;     ...
;     for (int i = 0; i < 8; ++i) { v[2 * i] = bflo(aw[i]) + bflo(bw[i]); v[2 * i + 1] = bfhi(aw[i]) + bfhi(bw[i]); ss += v[2 * i] * v[2 * i] + v[2 * i + 1] * v[2 * i + 1]; }
;     ss += __shfl_xor(ss, 1); ss += __shfl_xor(ss, 2); ss += __shfl_xor(ss, 4);
;     const float rstd = rsqrtf(ss * (1.f / DV) + EPS);
;     const bf16_t* gp = p.gate + (long)(NCTX + row) * 1024 + lane * 16;
;     const u32x4 g0 = *(const u32x4*)gp, g1 = *(const u32x4*)(gp + 8);
;     float gt[16]; gt[0] = bflo(g0.x); gt[1] = bfhi(g0.x); gt[2] = bflo(g0.y); gt[3] = bfhi(g0.y); gt[4] = bflo(g0.z); gt[5] = bfhi(g0.z); gt[6] = bflo(g0.w); gt[7] = bfhi(g0.w);
;     gt[8] = bflo(g1.x); gt[9] = bfhi(g1.x); gt[10] = bflo(g1.y); gt[11] = bfhi(g1.y); gt[12] = bflo(g1.z); gt[13] = bfhi(g1.z); gt[14] = bflo(g1.w); gt[15] = bfhi(g1.w);
;     const float* gn = p.g_norm + (lane & 7) * 16;
;     unsigned o[8];
; #pragma unroll
;     for (int j = 0; j < 8; ++j) o[j] = cvt_pk_bf16(v[2 * j] * rstd * gn[2 * j] * gt[2 * j], v[2 * j + 1] * rstd * gn[2 * j + 1] * gt[2 * j + 1]);
;     bf16_t* op = p.aout + (long)row * DM + 1024 + lane * 16;
;     *(u32x4*)op = (u32x4){o[0], o[1], o[2], o[3]}; *(u32x4*)(op + 8) = (u32x4){o[4], o[5], o[6], o[7]};
	v_add_f32_e32 v212, v212, v214
	v_add_f32_e32 v213, v213, v215
	v_mov_b32_e32 v214, 0x358637bd
	v_fmac_f32_e32 v214, 0x3c000000, v212
	v_mov_b32_e32 v215, 0x358637bd
	v_fmac_f32_e32 v215, 0x3c000000, v213
	v_rsq_f32_e32 v214, v214
	v_rsq_f32_e32 v215, v215
	s_lshl_b32 s22, s20, 12
	s_add_u32 s30, s4, s22
	s_addc_u32 s31, s5, 0
	v_lshlrev_b32_e32 v208, 16, v32
	v_and_b32_e32 v209, 0xffff0000, v32
	v_mul_f32_e32 v16, v16, v214
	v_mul_f32_e32 v24, v24, v214
	v_mul_f32_e32 v16, v16, v6
	v_mul_f32_e32 v24, v24, v7
	v_mul_f32_e32 v16, v16, v208
	v_mul_f32_e32 v24, v24, v209
	v_cvt_pk_bf16_f32 v32, v16, v24
	v_lshlrev_b32_e32 v208, 16, v33
	v_and_b32_e32 v209, 0xffff0000, v33
	v_mul_f32_e32 v17, v17, v214
	v_mul_f32_e32 v25, v25, v214
	v_mul_f32_e32 v17, v17, v8
	v_mul_f32_e32 v25, v25, v9
	v_mul_f32_e32 v17, v17, v208
	v_mul_f32_e32 v25, v25, v209
	v_cvt_pk_bf16_f32 v33, v17, v25
	v_lshlrev_b32_e32 v208, 16, v34
	v_and_b32_e32 v209, 0xffff0000, v34
	v_mul_f32_e32 v18, v18, v214
	v_mul_f32_e32 v26, v26, v214
	v_mul_f32_e32 v18, v18, v10
	v_mul_f32_e32 v26, v26, v11
	v_mul_f32_e32 v18, v18, v208
	v_mul_f32_e32 v26, v26, v209
	v_cvt_pk_bf16_f32 v34, v18, v26
	v_lshlrev_b32_e32 v208, 16, v35
	v_and_b32_e32 v209, 0xffff0000, v35
	v_mul_f32_e32 v19, v19, v214
	v_mul_f32_e32 v27, v27, v214
	v_mul_f32_e32 v19, v19, v12
	v_mul_f32_e32 v27, v27, v13
	v_mul_f32_e32 v19, v19, v208
	v_mul_f32_e32 v27, v27, v209
	v_cvt_pk_bf16_f32 v35, v19, v27
	global_store_dwordx4 v1, v[32:35], s[30:31] offset:2048
	v_lshlrev_b32_e32 v208, 16, v36
	v_and_b32_e32 v209, 0xffff0000, v36
	v_mul_f32_e32 v20, v20, v215
	v_mul_f32_e32 v28, v28, v215
	v_mul_f32_e32 v20, v20, v6
	v_mul_f32_e32 v28, v28, v7
	v_mul_f32_e32 v20, v20, v208
	v_mul_f32_e32 v28, v28, v209
	v_cvt_pk_bf16_f32 v36, v20, v28
	v_lshlrev_b32_e32 v208, 16, v37
	v_and_b32_e32 v209, 0xffff0000, v37
	v_mul_f32_e32 v21, v21, v215
	v_mul_f32_e32 v29, v29, v215
	v_mul_f32_e32 v21, v21, v8
	v_mul_f32_e32 v29, v29, v9
	v_mul_f32_e32 v21, v21, v208
	v_mul_f32_e32 v29, v29, v209
	v_cvt_pk_bf16_f32 v37, v21, v29
	v_lshlrev_b32_e32 v208, 16, v38
	v_and_b32_e32 v209, 0xffff0000, v38
	v_mul_f32_e32 v22, v22, v215
	v_mul_f32_e32 v30, v30, v215
	v_mul_f32_e32 v22, v22, v10
	v_mul_f32_e32 v30, v30, v11
	v_mul_f32_e32 v22, v22, v208
	v_mul_f32_e32 v30, v30, v209
	v_cvt_pk_bf16_f32 v38, v22, v30
	v_lshlrev_b32_e32 v208, 16, v39
	v_and_b32_e32 v209, 0xffff0000, v39
	v_mul_f32_e32 v23, v23, v215
	v_mul_f32_e32 v31, v31, v215
	v_mul_f32_e32 v23, v23, v12
	v_mul_f32_e32 v31, v31, v13
	v_mul_f32_e32 v23, v23, v208
	v_mul_f32_e32 v31, v31, v209
	v_cvt_pk_bf16_f32 v39, v23, v31
	global_store_dwordx4 v1, v[36:39], s[30:31] offset:3072
	s_branch .Lp5c_end
.Lp5c_a_next:
.Lp5c_b:
	s_add_u32 s23, s20, s21
	s_cmp_lt_u32 s23, 0x4000
	s_cbranch_scc0 .Lp5c_b_last
	s_lshl_b32 s22, s23, 11
	s_add_u32 s24, s6, s22
	s_addc_u32 s25, s7, 0
	s_add_u32 s26, s12, s22
	s_addc_u32 s27, s13, 0
	s_add_u32 s28, s14, s22
	s_addc_u32 s29, s15, 0
	s_add_u32 s28, s28, 0x200000
	s_addc_u32 s29, s29, 0
	global_load_dwordx4 v[16:19], v1, s[24:25] offset:0
	global_load_dwordx4 v[20:23], v1, s[24:25] offset:1024
	global_load_dwordx4 v[24:27], v1, s[26:27] offset:0
	global_load_dwordx4 v[28:31], v1, s[26:27] offset:1024
	global_load_dwordx4 v[32:35], v1, s[28:29] offset:0
	global_load_dwordx4 v[36:39], v1, s[28:29] offset:1024
	s_waitcnt vmcnt(6)
	v_lshlrev_b32_e32 v208, 16, v40
	v_lshlrev_b32_e32 v209, 16, v48
	v_and_b32_e32 v210, 0xffff0000, v40
	v_and_b32_e32 v211, 0xffff0000, v48
	v_add_f32_e32 v40, v208, v209
	v_add_f32_e32 v48, v210, v211
	v_lshlrev_b32_e32 v208, 16, v41
	v_lshlrev_b32_e32 v209, 16, v49
	v_and_b32_e32 v210, 0xffff0000, v41
	v_and_b32_e32 v211, 0xffff0000, v49
	v_add_f32_e32 v41, v208, v209
	v_add_f32_e32 v49, v210, v211
	v_lshlrev_b32_e32 v208, 16, v42
	v_lshlrev_b32_e32 v209, 16, v50
	v_and_b32_e32 v210, 0xffff0000, v42
	v_and_b32_e32 v211, 0xffff0000, v50
	v_add_f32_e32 v42, v208, v209
	v_add_f32_e32 v50, v210, v211
	v_lshlrev_b32_e32 v208, 16, v43
	v_lshlrev_b32_e32 v209, 16, v51
	v_and_b32_e32 v210, 0xffff0000, v43
	v_and_b32_e32 v211, 0xffff0000, v51
	v_add_f32_e32 v43, v208, v209
	v_add_f32_e32 v51, v210, v211
	v_mul_f32_e32 v212, v40, v40
	v_fmac_f32_e32 v212, v48, v48
	v_fmac_f32_e32 v212, v41, v41
	v_fmac_f32_e32 v212, v49, v49
	v_fmac_f32_e32 v212, v42, v42
	v_fmac_f32_e32 v212, v50, v50
	v_fmac_f32_e32 v212, v43, v43
	v_fmac_f32_e32 v212, v51, v51
	v_lshlrev_b32_e32 v208, 16, v44
	v_lshlrev_b32_e32 v209, 16, v52
	v_and_b32_e32 v210, 0xffff0000, v44
	v_and_b32_e32 v211, 0xffff0000, v52
	v_add_f32_e32 v44, v208, v209
	v_add_f32_e32 v52, v210, v211
	v_lshlrev_b32_e32 v208, 16, v45
	v_lshlrev_b32_e32 v209, 16, v53
	v_and_b32_e32 v210, 0xffff0000, v45
	v_and_b32_e32 v211, 0xffff0000, v53
	v_add_f32_e32 v45, v208, v209
	v_add_f32_e32 v53, v210, v211
	v_lshlrev_b32_e32 v208, 16, v46
	v_lshlrev_b32_e32 v209, 16, v54
	v_and_b32_e32 v210, 0xffff0000, v46
	v_and_b32_e32 v211, 0xffff0000, v54
	v_add_f32_e32 v46, v208, v209
	v_add_f32_e32 v54, v210, v211
	v_lshlrev_b32_e32 v208, 16, v47
	v_lshlrev_b32_e32 v209, 16, v55
	v_and_b32_e32 v210, 0xffff0000, v47
	v_and_b32_e32 v211, 0xffff0000, v55
	v_add_f32_e32 v47, v208, v209
	v_add_f32_e32 v55, v210, v211
	v_mul_f32_e32 v213, v44, v44
	v_fmac_f32_e32 v213, v52, v52
	v_fmac_f32_e32 v213, v45, v45
	v_fmac_f32_e32 v213, v53, v53
	v_fmac_f32_e32 v213, v46, v46
	v_fmac_f32_e32 v213, v54, v54
	v_fmac_f32_e32 v213, v47, v47
	v_fmac_f32_e32 v213, v55, v55
	ds_bpermute_b32 v214, v2, v212
	ds_bpermute_b32 v215, v2, v213
	s_waitcnt lgkmcnt(0)
; DEV unsigned cvt_pk_bf16(float lo, float hi) { const f32x2 v = {lo, hi}; const bf16n2 r = __builtin_convertvector(v, bf16n2); return __builtin_bit_cast(unsigned, r); }
; DEV float bflo(unsigned v) { return __uint_as_float(v << 16); }
; DEV float bfhi(unsigned v) { return __uint_as_float(v & 0xffff0000u); }
; DEV void phase5c_rec(CParams& p, int wg, int nwg) {
;     ...
;   for (int row = wg * 8 + wid; row < NLAT; row += nwg * 8) {
;     const bf16_t* a = p.of + (long)row * 1024 + lane * 16; const bf16_t* b = p.ob + (long)row * 1024 + lane * 16;
;     const u32x4 a0 = *(const u32x4*)a, a1 = *(const u32x4*)(a + 8), b0 = *(const u32x4*)b, b1 = *(const u32x4*)(b + 8);
;     const unsigned aw[8] = {a0.x, a0.y, a0.z, a0.w, a1.x, a1.y, a1.z, a1.w}, bw[8] = {b0.x, b0.y, b0.z, b0.w, b1.x, b1.y, b1.z, b1.w};
;     float v[16]; float ss = 0.f;
; #pragma unroll
;     for (int i = 0; i < 8; ++i) { v[2 * i] = bflo(aw[i]) + bflo(bw[i]); v[2 * i + 1] = bfhi(aw[i]) + bfhi(bw[i]); ss += v[2 * i] * v[2 * i] + v[2 * i + 1] * v[2 * i + 1]; }
;     ss += __shfl_xor(ss, 1); ss += __shfl_xor(ss, 2); ss += __shfl_xor(ss, 4);
;     const float rstd = rsqrtf(ss * (1.f / DV) + EPS);
;     const bf16_t* gp = p.gate + (long)(NCTX + row) * 1024 + lane * 16;
;     const u32x4 g0 = *(const u32x4*)gp, g1 = *(const u32x4*)(gp + 8);
;     float gt[16]; gt[0] = bflo(g0.x); gt[1] = bfhi(g0.x); gt[2] = bflo(g0.y); gt[3] = bfhi(g0.y); gt[4] = bflo(g0.z); gt[5] = bfhi(g0.z); gt[6] = bflo(g0.w); gt[7] = bfhi(g0.w);
;     gt[8] = bflo(g1.x); gt[9] = bfhi(g1.x); gt[10] = bflo(g1.y); gt[11] = bfhi(g1.y); gt[12] = bflo(g1.z); gt[13] = bfhi(g1.z); gt[14] = bflo(g1.w); gt[15] = bfhi(g1.w);
;     const float* gn = p.g_norm + (lane & 7) * 16;
;     unsigned o[8];
; #pragma unroll
;     for (int j = 0; j < 8; ++j) o[j] = cvt_pk_bf16(v[2 * j] * rstd * gn[2 * j] * gt[2 * j], v[2 * j + 1] * rstd * gn[2 * j + 1] * gt[2 * j + 1]);
;     bf16_t* op = p.aout + (long)row * DM + 1024 + lane * 16;
;     *(u32x4*)op = (u32x4){o[0], o[1], o[2], o[3]}; *(u32x4*)(op + 8) = (u32x4){o[4], o[5], o[6], o[7]};
	v_add_f32_e32 v212, v212, v214
	v_add_f32_e32 v213, v213, v215
	ds_bpermute_b32 v214, v3, v212
	ds_bpermute_b32 v215, v3, v213
	s_waitcnt lgkmcnt(0)
	v_add_f32_e32 v212, v212, v214
	v_add_f32_e32 v213, v213, v215
	ds_bpermute_b32 v214, v4, v212
	ds_bpermute_b32 v215, v4, v213
	s_waitcnt lgkmcnt(0)
	v_add_f32_e32 v212, v212, v214
	v_add_f32_e32 v213, v213, v215
	ds_bpermute_b32 v214, v5, v212
	ds_bpermute_b32 v215, v5, v213
	s_waitcnt lgkmcnt(0)
	v_add_f32_e32 v212, v212, v214
	v_add_f32_e32 v213, v213, v215
	v_mov_b32_e32 v214, 0x358637bd
	v_fmac_f32_e32 v214, 0x3c000000, v212
	v_mov_b32_e32 v215, 0x358637bd
	v_fmac_f32_e32 v215, 0x3c000000, v213
	v_rsq_f32_e32 v214, v214
	v_rsq_f32_e32 v215, v215
	s_lshl_b32 s22, s20, 12
	s_add_u32 s30, s4, s22
	s_addc_u32 s31, s5, 0
	v_lshlrev_b32_e32 v208, 16, v56
	v_and_b32_e32 v209, 0xffff0000, v56
	v_mul_f32_e32 v40, v40, v214
	v_mul_f32_e32 v48, v48, v214
	v_mul_f32_e32 v40, v40, v6
	v_mul_f32_e32 v48, v48, v7
	v_mul_f32_e32 v40, v40, v208
	v_mul_f32_e32 v48, v48, v209
	v_cvt_pk_bf16_f32 v56, v40, v48
	v_lshlrev_b32_e32 v208, 16, v57
	v_and_b32_e32 v209, 0xffff0000, v57
	v_mul_f32_e32 v41, v41, v214
	v_mul_f32_e32 v49, v49, v214
	v_mul_f32_e32 v41, v41, v8
	v_mul_f32_e32 v49, v49, v9
	v_mul_f32_e32 v41, v41, v208
	v_mul_f32_e32 v49, v49, v209
	v_cvt_pk_bf16_f32 v57, v41, v49
	v_lshlrev_b32_e32 v208, 16, v58
	v_and_b32_e32 v209, 0xffff0000, v58
	v_mul_f32_e32 v42, v42, v214
	v_mul_f32_e32 v50, v50, v214
	v_mul_f32_e32 v42, v42, v10
	v_mul_f32_e32 v50, v50, v11
	v_mul_f32_e32 v42, v42, v208
	v_mul_f32_e32 v50, v50, v209
	v_cvt_pk_bf16_f32 v58, v42, v50
	v_lshlrev_b32_e32 v208, 16, v59
	v_and_b32_e32 v209, 0xffff0000, v59
	v_mul_f32_e32 v43, v43, v214
	v_mul_f32_e32 v51, v51, v214
	v_mul_f32_e32 v43, v43, v12
	v_mul_f32_e32 v51, v51, v13
	v_mul_f32_e32 v43, v43, v208
	v_mul_f32_e32 v51, v51, v209
	v_cvt_pk_bf16_f32 v59, v43, v51
	global_store_dwordx4 v1, v[56:59], s[30:31] offset:2048
	v_lshlrev_b32_e32 v208, 16, v60
	v_and_b32_e32 v209, 0xffff0000, v60
	v_mul_f32_e32 v44, v44, v215
	v_mul_f32_e32 v52, v52, v215
	v_mul_f32_e32 v44, v44, v6
	v_mul_f32_e32 v52, v52, v7
	v_mul_f32_e32 v44, v44, v208
	v_mul_f32_e32 v52, v52, v209
	v_cvt_pk_bf16_f32 v60, v44, v52
	v_lshlrev_b32_e32 v208, 16, v61
	v_and_b32_e32 v209, 0xffff0000, v61
	v_mul_f32_e32 v45, v45, v215
	v_mul_f32_e32 v53, v53, v215
	v_mul_f32_e32 v45, v45, v8
	v_mul_f32_e32 v53, v53, v9
	v_mul_f32_e32 v45, v45, v208
	v_mul_f32_e32 v53, v53, v209
	v_cvt_pk_bf16_f32 v61, v45, v53
	v_lshlrev_b32_e32 v208, 16, v62
	v_and_b32_e32 v209, 0xffff0000, v62
	v_mul_f32_e32 v46, v46, v215
	v_mul_f32_e32 v54, v54, v215
	v_mul_f32_e32 v46, v46, v10
	v_mul_f32_e32 v54, v54, v11
	v_mul_f32_e32 v46, v46, v208
	v_mul_f32_e32 v54, v54, v209
	v_cvt_pk_bf16_f32 v62, v46, v54
	v_lshlrev_b32_e32 v208, 16, v63
	v_and_b32_e32 v209, 0xffff0000, v63
	v_mul_f32_e32 v47, v47, v215
	v_mul_f32_e32 v55, v55, v215
	v_mul_f32_e32 v47, v47, v12
	v_mul_f32_e32 v55, v55, v13
	v_mul_f32_e32 v47, v47, v208
	v_mul_f32_e32 v55, v55, v209
	v_cvt_pk_bf16_f32 v63, v47, v55
	global_store_dwordx4 v1, v[60:63], s[30:31] offset:3072
	s_mov_b32 s20, s23
	s_branch .Lp5c_b_next
; DEV unsigned cvt_pk_bf16(float lo, float hi) { const f32x2 v = {lo, hi}; const bf16n2 r = __builtin_convertvector(v, bf16n2); return __builtin_bit_cast(unsigned, r); }
; DEV float bflo(unsigned v) { return __uint_as_float(v << 16); }
; DEV float bfhi(unsigned v) { return __uint_as_float(v & 0xffff0000u); }
; DEV void phase5c_rec(CParams& p, int wg, int nwg) {
;     ...
;     for (int i = 0; i < 8; ++i) { v[2 * i] = bflo(aw[i]) + bflo(bw[i]); v[2 * i + 1] = bfhi(aw[i]) + bfhi(bw[i]); ss += v[2 * i] * v[2 * i] + v[2 * i + 1] * v[2 * i + 1]; }
;     ss += __shfl_xor(ss, 1); ss += __shfl_xor(ss, 2); ss += __shfl_xor(ss, 4);
;     const float rstd = rsqrtf(ss * (1.f / DV) + EPS);
;     const bf16_t* gp = p.gate + (long)(NCTX + row) * 1024 + lane * 16;
;     const u32x4 g0 = *(const u32x4*)gp, g1 = *(const u32x4*)(gp + 8);
;     float gt[16]; gt[0] = bflo(g0.x); gt[1] = bfhi(g0.x); gt[2] = bflo(g0.y); gt[3] = bfhi(g0.y); gt[4] = bflo(g0.z); gt[5] = bfhi(g0.z); gt[6] = bflo(g0.w); gt[7] = bfhi(g0.w);
;     gt[8] = bflo(g1.x); gt[9] = bfhi(g1.x); gt[10] = bflo(g1.y); gt[11] = bfhi(g1.y); gt[12] = bflo(g1.z); gt[13] = bfhi(g1.z); gt[14] = bflo(g1.w); gt[15] = bfhi(g1.w);
;     const float* gn = p.g_norm + (lane & 7) * 16;
;     unsigned o[8];
; #pragma unroll
;     for (int j = 0; j < 8; ++j) o[j] = cvt_pk_bf16(v[2 * j] * rstd * gn[2 * j] * gt[2 * j], v[2 * j + 1] * rstd * gn[2 * j + 1] * gt[2 * j + 1]);
;     bf16_t* op = p.aout + (long)row * DM + 1024 + lane * 16;
;     *(u32x4*)op = (u32x4){o[0], o[1], o[2], o[3]}; *(u32x4*)(op + 8) = (u32x4){o[4], o[5], o[6], o[7]};
; __device__ __forceinline__ void xcd_barrier(const XcdBarrier& b) {
;     asm volatile("s_waitcnt vmcnt(0)" ::: "memory");
;     __syncthreads();
;     if (threadIdx.x == 0) {
;         unsigned* bar = b.bar;
;         __builtin_amdgcn_s_waitcnt(0);
;         unsigned nloc = b.st[0], nx = b.st[1];
;         if (nloc == 0u) { xcd_barrier_complete(bar, b.x, nloc, nx); b.st[0] = nloc; b.st[1] = nx; }
.Lp5c_b_last:
	s_waitcnt vmcnt(0)
	v_lshlrev_b32_e32 v208, 16, v40
	v_lshlrev_b32_e32 v209, 16, v48
	v_and_b32_e32 v210, 0xffff0000, v40
	v_and_b32_e32 v211, 0xffff0000, v48
	v_add_f32_e32 v40, v208, v209
	v_add_f32_e32 v48, v210, v211
	v_lshlrev_b32_e32 v208, 16, v41
	v_lshlrev_b32_e32 v209, 16, v49
	v_and_b32_e32 v210, 0xffff0000, v41
	v_and_b32_e32 v211, 0xffff0000, v49
	v_add_f32_e32 v41, v208, v209
	v_add_f32_e32 v49, v210, v211
	v_lshlrev_b32_e32 v208, 16, v42
	v_lshlrev_b32_e32 v209, 16, v50
	v_and_b32_e32 v210, 0xffff0000, v42
	v_and_b32_e32 v211, 0xffff0000, v50
	v_add_f32_e32 v42, v208, v209
	v_add_f32_e32 v50, v210, v211
	v_lshlrev_b32_e32 v208, 16, v43
	v_lshlrev_b32_e32 v209, 16, v51
	v_and_b32_e32 v210, 0xffff0000, v43
	v_and_b32_e32 v211, 0xffff0000, v51
	v_add_f32_e32 v43, v208, v209
	v_add_f32_e32 v51, v210, v211
	v_mul_f32_e32 v212, v40, v40
	v_fmac_f32_e32 v212, v48, v48
	v_fmac_f32_e32 v212, v41, v41
	v_fmac_f32_e32 v212, v49, v49
	v_fmac_f32_e32 v212, v42, v42
	v_fmac_f32_e32 v212, v50, v50
	v_fmac_f32_e32 v212, v43, v43
	v_fmac_f32_e32 v212, v51, v51
	v_lshlrev_b32_e32 v208, 16, v44
	v_lshlrev_b32_e32 v209, 16, v52
	v_and_b32_e32 v210, 0xffff0000, v44
	v_and_b32_e32 v211, 0xffff0000, v52
	v_add_f32_e32 v44, v208, v209
	v_add_f32_e32 v52, v210, v211
	v_lshlrev_b32_e32 v208, 16, v45
	v_lshlrev_b32_e32 v209, 16, v53
	v_and_b32_e32 v210, 0xffff0000, v45
	v_and_b32_e32 v211, 0xffff0000, v53
	v_add_f32_e32 v45, v208, v209
	v_add_f32_e32 v53, v210, v211
	v_lshlrev_b32_e32 v208, 16, v46
	v_lshlrev_b32_e32 v209, 16, v54
	v_and_b32_e32 v210, 0xffff0000, v46
	v_and_b32_e32 v211, 0xffff0000, v54
	v_add_f32_e32 v46, v208, v209
	v_add_f32_e32 v54, v210, v211
	v_lshlrev_b32_e32 v208, 16, v47
	v_lshlrev_b32_e32 v209, 16, v55
	v_and_b32_e32 v210, 0xffff0000, v47
	v_and_b32_e32 v211, 0xffff0000, v55
	v_add_f32_e32 v47, v208, v209
	v_add_f32_e32 v55, v210, v211
	v_mul_f32_e32 v213, v44, v44
	v_fmac_f32_e32 v213, v52, v52
	v_fmac_f32_e32 v213, v45, v45
	v_fmac_f32_e32 v213, v53, v53
	v_fmac_f32_e32 v213, v46, v46
	v_fmac_f32_e32 v213, v54, v54
	v_fmac_f32_e32 v213, v47, v47
	v_fmac_f32_e32 v213, v55, v55
	ds_bpermute_b32 v214, v2, v212
	ds_bpermute_b32 v215, v2, v213
	s_waitcnt lgkmcnt(0)
	v_add_f32_e32 v212, v212, v214
	v_add_f32_e32 v213, v213, v215
	ds_bpermute_b32 v214, v3, v212
	ds_bpermute_b32 v215, v3, v213
	s_waitcnt lgkmcnt(0)
	v_add_f32_e32 v212, v212, v214
	v_add_f32_e32 v213, v213, v215
	ds_bpermute_b32 v214, v4, v212
	ds_bpermute_b32 v215, v4, v213
	s_waitcnt lgkmcnt(0)
	v_add_f32_e32 v212, v212, v214
	v_add_f32_e32 v213, v213, v215
	ds_bpermute_b32 v214, v5, v212
	ds_bpermute_b32 v215, v5, v213
	s_waitcnt lgkmcnt(0)
	v_add_f32_e32 v212, v212, v214
	v_add_f32_e32 v213, v213, v215
	v_mov_b32_e32 v214, 0x358637bd
	v_fmac_f32_e32 v214, 0x3c000000, v212
	v_mov_b32_e32 v215, 0x358637bd
	v_fmac_f32_e32 v215, 0x3c000000, v213
	v_rsq_f32_e32 v214, v214
	v_rsq_f32_e32 v215, v215
	s_lshl_b32 s22, s20, 12
	s_add_u32 s30, s4, s22
	s_addc_u32 s31, s5, 0
	v_lshlrev_b32_e32 v208, 16, v56
	v_and_b32_e32 v209, 0xffff0000, v56
	v_mul_f32_e32 v40, v40, v214
	v_mul_f32_e32 v48, v48, v214
	v_mul_f32_e32 v40, v40, v6
	v_mul_f32_e32 v48, v48, v7
	v_mul_f32_e32 v40, v40, v208
	v_mul_f32_e32 v48, v48, v209
	v_cvt_pk_bf16_f32 v56, v40, v48
	v_lshlrev_b32_e32 v208, 16, v57
	v_and_b32_e32 v209, 0xffff0000, v57
	v_mul_f32_e32 v41, v41, v214
	v_mul_f32_e32 v49, v49, v214
	v_mul_f32_e32 v41, v41, v8
	v_mul_f32_e32 v49, v49, v9
	v_mul_f32_e32 v41, v41, v208
	v_mul_f32_e32 v49, v49, v209
	v_cvt_pk_bf16_f32 v57, v41, v49
	v_lshlrev_b32_e32 v208, 16, v58
	v_and_b32_e32 v209, 0xffff0000, v58
	v_mul_f32_e32 v42, v42, v214
	v_mul_f32_e32 v50, v50, v214
	v_mul_f32_e32 v42, v42, v10
	v_mul_f32_e32 v50, v50, v11
	v_mul_f32_e32 v42, v42, v208
	v_mul_f32_e32 v50, v50, v209
	v_cvt_pk_bf16_f32 v58, v42, v50
	v_lshlrev_b32_e32 v208, 16, v59
	v_and_b32_e32 v209, 0xffff0000, v59
	v_mul_f32_e32 v43, v43, v214
	v_mul_f32_e32 v51, v51, v214
	v_mul_f32_e32 v43, v43, v12
	v_mul_f32_e32 v51, v51, v13
	v_mul_f32_e32 v43, v43, v208
	v_mul_f32_e32 v51, v51, v209
	v_cvt_pk_bf16_f32 v59, v43, v51
	global_store_dwordx4 v1, v[56:59], s[30:31] offset:2048
	v_lshlrev_b32_e32 v208, 16, v60
	v_and_b32_e32 v209, 0xffff0000, v60
	v_mul_f32_e32 v44, v44, v215
	v_mul_f32_e32 v52, v52, v215
	v_mul_f32_e32 v44, v44, v6
	v_mul_f32_e32 v52, v52, v7
	v_mul_f32_e32 v44, v44, v208
	v_mul_f32_e32 v52, v52, v209
	v_cvt_pk_bf16_f32 v60, v44, v52
	v_lshlrev_b32_e32 v208, 16, v61
	v_and_b32_e32 v209, 0xffff0000, v61
	v_mul_f32_e32 v45, v45, v215
	v_mul_f32_e32 v53, v53, v215
	v_mul_f32_e32 v45, v45, v8
	v_mul_f32_e32 v53, v53, v9
	v_mul_f32_e32 v45, v45, v208
	v_mul_f32_e32 v53, v53, v209
	v_cvt_pk_bf16_f32 v61, v45, v53
	v_lshlrev_b32_e32 v208, 16, v62
	v_and_b32_e32 v209, 0xffff0000, v62
	v_mul_f32_e32 v46, v46, v215
	v_mul_f32_e32 v54, v54, v215
	v_mul_f32_e32 v46, v46, v10
	v_mul_f32_e32 v54, v54, v11
	v_mul_f32_e32 v46, v46, v208
	v_mul_f32_e32 v54, v54, v209
	v_cvt_pk_bf16_f32 v62, v46, v54
	v_lshlrev_b32_e32 v208, 16, v63
	v_and_b32_e32 v209, 0xffff0000, v63
	v_mul_f32_e32 v47, v47, v215
	v_mul_f32_e32 v55, v55, v215
	v_mul_f32_e32 v47, v47, v12
	v_mul_f32_e32 v55, v55, v13
	v_mul_f32_e32 v47, v47, v208
	v_mul_f32_e32 v55, v55, v209
	v_cvt_pk_bf16_f32 v63, v47, v55
	global_store_dwordx4 v1, v[60:63], s[30:31] offset:3072
	s_branch .Lp5c_end
.Lp5c_b_next:
	s_branch .Lp5c_a
.Lp5c_end:
.LBB0_1186:
	s_or_b64 exec, exec, s[8:9]
	s_waitcnt vmcnt(0)
	s_barrier
	s_and_saveexec_b64 s[4:5], s[40:41]
	s_cbranch_execz .LBB0_1238
	s_add_i32 s3, 0, 0x27ff0
	v_mov_b32_e32 v1, s3
	s_waitcnt vmcnt(0) expcnt(0) lgkmcnt(0)
	ds_read_b32 v3, v1
	s_add_i32 s3, 0, 0x27ff4
	v_mov_b32_e32 v1, s3
	ds_read_b32 v1, v1
	s_waitcnt lgkmcnt(1)
	v_cmp_ne_u32_e32 vcc, 0, v3
	s_cbranch_vccnz .LBB0_1202
	s_load_dwordx2 s[10:11], s[48:49], 0x4
	s_add_u32 s6, s42, 0x1000
	s_addc_u32 s7, s43, 0
	s_add_u32 s8, s42, 0x1100
	s_addc_u32 s9, s43, 0
	s_waitcnt lgkmcnt(0)
	s_mul_i32 s3, s10, s33
	s_add_u32 s10, s42, 0x1200
	s_mul_i32 s3, s3, s11
	s_addc_u32 s11, s43, 0
	s_add_u32 s12, s42, 0x1300
	s_addc_u32 s13, s43, 0
	s_mov_b32 s20, 1
	v_mov_b32_e32 v17, 0
	s_branch .LBB0_1190
